# speedup vs baseline: 1.0032x; 1.0032x over previous
.LBB0_6:
	s_load_dwordx4 s[12:15], s[0:1], 0x10
	s_load_dwordx2 s[16:17], s[0:1], 0x20
	v_and_b32_e32 v33, 15, v0
	v_bfe_u32 v32, v0, 4, 2
	v_mov_b32_e32 v1, 0
	v_accvgpr_write_b32 a0, 0
	v_accvgpr_write_b32 a1, 0
	v_accvgpr_write_b32 a2, 0
	v_accvgpr_write_b32 a3, 0
	v_accvgpr_write_b32 a4, 0
	v_accvgpr_write_b32 a5, 0
	v_accvgpr_write_b32 a6, 0
	v_accvgpr_write_b32 a7, 0
	v_accvgpr_write_b32 a8, 0
	v_accvgpr_write_b32 a9, 0
	v_accvgpr_write_b32 a10, 0
	v_accvgpr_write_b32 a11, 0
	v_accvgpr_write_b32 a12, 0
	v_accvgpr_write_b32 a13, 0
	v_accvgpr_write_b32 a14, 0
	s_andn2_b64 vcc, exec, s[18:19]
	v_accvgpr_write_b32 a15, 0
	s_cbranch_vccnz .LBB0_16
	v_lshrrev_b32_e32 v44, 4, v0
	v_and_b32_e32 v36, 0x78, v4
	v_or_b32_e32 v4, s20, v44
	v_min_i32_e32 v0, s25, v4
	v_mad_i64_i32 v[2:3], s[0:1], v0, s10, 0
	v_or_b32_e32 v5, s22, v44
	s_waitcnt lgkmcnt(0)
	v_lshl_add_u64 v[2:3], v[2:3], 1, s[4:5]
	v_lshlrev_b32_e32 v0, 1, v36
	v_lshl_add_u64 v[16:17], v[2:3], 0, v[0:1]
	v_min_i32_e32 v2, s24, v5
	v_mad_i64_i32 v[2:3], s[0:1], v2, s10, 0
	v_lshl_add_u64 v[2:3], v[2:3], 1, s[6:7]
	v_lshl_add_u64 v[18:19], v[2:3], 0, v[0:1]
	v_add_u32_e32 v2, 16, v4
	v_min_i32_e32 v2, s25, v2
	v_mad_i64_i32 v[2:3], s[0:1], v2, s10, 0
	v_lshl_add_u64 v[2:3], v[2:3], 1, s[4:5]
	v_lshl_add_u64 v[20:21], v[2:3], 0, v[0:1]
	v_add_u32_e32 v2, 16, v5
	v_min_i32_e32 v2, s24, v2
	v_mad_i64_i32 v[2:3], s[0:1], v2, s10, 0
	v_lshl_add_u64 v[2:3], v[2:3], 1, s[6:7]
	v_lshl_add_u64 v[22:23], v[2:3], 0, v[0:1]
	v_add_u32_e32 v2, 32, v4
	v_min_i32_e32 v2, s25, v2
	v_mad_i64_i32 v[2:3], s[0:1], v2, s10, 0
	v_lshl_add_u64 v[2:3], v[2:3], 1, s[4:5]
	v_lshl_add_u64 v[24:25], v[2:3], 0, v[0:1]
	v_add_u32_e32 v2, 32, v5
	v_min_i32_e32 v2, s24, v2
	v_mad_i64_i32 v[2:3], s[0:1], v2, s10, 0
	v_lshl_add_u64 v[2:3], v[2:3], 1, s[6:7]
	v_lshl_add_u64 v[26:27], v[2:3], 0, v[0:1]
	v_add_u32_e32 v2, 48, v4
	v_min_i32_e32 v2, s25, v2
	v_mad_i64_i32 v[2:3], s[0:1], v2, s10, 0
	v_lshl_add_u64 v[2:3], v[2:3], 1, s[4:5]
	v_lshl_add_u64 v[28:29], v[2:3], 0, v[0:1]
	v_add_u32_e32 v2, 48, v5
	v_min_i32_e32 v2, s24, v2
	v_mad_i64_i32 v[2:3], s[0:1], v2, s10, 0
	v_add_u32_e32 v37, s26, v36
	s_add_i32 s18, s11, -8
	v_lshl_add_u64 v[2:3], v[2:3], 1, s[6:7]
	v_lshl_add_u64 v[30:31], v[2:3], 0, v[0:1]
	v_min_i32_e32 v0, s18, v37
	v_sub_u32_e32 v0, v0, v36
	v_ashrrev_i32_e32 v1, 31, v0
	v_lshlrev_b64 v[8:9], 1, v[0:1]
	v_lshl_add_u64 v[0:1], v[18:19], 0, v[8:9]
	v_lshl_add_u64 v[2:3], v[22:23], 0, v[8:9]
	global_load_dwordx4 v[54:57], v[0:1], off
	global_load_dwordx4 v[58:61], v[2:3], off
	v_lshl_add_u64 v[0:1], v[26:27], 0, v[8:9]
	v_lshl_add_u64 v[2:3], v[30:31], 0, v[8:9]
	v_lshl_add_u64 v[10:11], v[16:17], 0, v[8:9]
	v_lshl_add_u64 v[12:13], v[20:21], 0, v[8:9]
	v_lshl_add_u64 v[40:41], v[24:25], 0, v[8:9]
	global_load_dwordx4 v[62:65], v[0:1], off
	global_load_dwordx4 v[66:69], v[2:3], off
	s_nop 0
	global_load_dwordx4 v[0:3], v[10:11], off
	global_load_dwordx4 v[4:7], v[12:13], off
	v_lshl_add_u64 v[42:43], v[28:29], 0, v[8:9]
	global_load_dwordx4 v[8:11], v[40:41], off
	global_load_dwordx4 v[12:15], v[42:43], off
	v_accvgpr_write_b32 a0, 0
	v_mul_u32_u24_e32 v38, 0xa8, v38
	v_or_b32_e32 v43, v34, v33
	v_mul_u32_u24_e32 v40, 0xa8, v44
	v_accvgpr_mov_b32 a3, a0
	v_add_lshl_u32 v38, v38, v39, 1
	s_movk_i32 s4, 0x5400
	v_or_b32_e32 v42, v35, v33
	v_add_lshl_u32 v40, v40, v36, 1
	s_movk_i32 s5, 0x150
	v_mul_u32_u24_e32 v43, 0x150, v43
	v_lshlrev_b32_e32 v44, 4, v32
	v_accvgpr_mov_b32 a1, a0
	v_accvgpr_mov_b32 a2, a0
	v_accvgpr_mov_b32 a7, a3
	v_accvgpr_mov_b32 a11, a3
	v_accvgpr_mov_b32 a15, a3
	v_cmp_gt_i32_e64 s[0:1], s11, v37
	s_add_i32 s6, s23, -1
	v_add_u32_e32 v39, 0x5400, v38
	v_add_u32_e32 v41, 0x5400, v40
	v_mad_u32_u24 v42, v42, s5, v44
	v_add3_u32 v43, v43, v44, s4
	s_mov_b32 s7, 0
	v_accvgpr_mov_b32 a6, a2
	v_accvgpr_mov_b32 a5, a1
	v_accvgpr_mov_b32 a4, a0
	v_accvgpr_mov_b32 a10, a2
	v_accvgpr_mov_b32 a9, a1
	v_accvgpr_mov_b32 a8, a0
	v_accvgpr_mov_b32 a14, a2
	v_accvgpr_mov_b32 a13, a1
	v_accvgpr_mov_b32 a12, a0
	v_min_i32_e32 v44, s18, v37
	v_sub_u32_e32 v44, v44, v36
	v_ashrrev_i32_e32 v45, 31, v44
	v_lshlrev_b64 v[44:45], 1, v[44:45]
	v_lshl_add_u64 v[18:19], v[18:19], 0, v[44:45]
	v_lshl_add_u64 v[22:23], v[22:23], 0, v[44:45]
	v_lshl_add_u64 v[26:27], v[26:27], 0, v[44:45]
	v_lshl_add_u64 v[30:31], v[30:31], 0, v[44:45]
	v_lshl_add_u64 v[16:17], v[16:17], 0, v[44:45]
	v_lshl_add_u64 v[20:21], v[20:21], 0, v[44:45]
	v_lshl_add_u64 v[24:25], v[24:25], 0, v[44:45]
	v_lshl_add_u64 v[28:29], v[28:29], 0, v[44:45]
	global_load_dwordx4 v[104:107], v[18:19], off offset:256
	global_load_dwordx4 v[108:111], v[22:23], off offset:256
	global_load_dwordx4 v[112:115], v[26:27], off offset:256
	global_load_dwordx4 v[116:119], v[30:31], off offset:256
	global_load_dwordx4 v[88:91], v[16:17], off offset:256
	global_load_dwordx4 v[92:95], v[20:21], off offset:256
	global_load_dwordx4 v[96:99], v[24:25], off offset:256
	global_load_dwordx4 v[100:103], v[28:29], off offset:256
	s_waitcnt vmcnt(14)
	ds_write_b128 v41, v[54:57]
	ds_write_b128 v41, v[58:61] offset:5376
	s_waitcnt vmcnt(12)
	ds_write_b128 v41, v[62:65] offset:10752
	ds_write_b128 v41, v[66:69] offset:16128
	s_waitcnt vmcnt(10)
	ds_write_b128 v40, v[0:3]
	ds_write_b128 v40, v[4:7] offset:5376
	s_waitcnt vmcnt(8)
	ds_write_b128 v40, v[8:11] offset:10752
	ds_write_b128 v40, v[12:15] offset:16128
	s_waitcnt lgkmcnt(0)
	s_barrier
	global_load_dwordx4 v[54:57], v[18:19], off offset:512
	global_load_dwordx4 v[58:61], v[22:23], off offset:512
	global_load_dwordx4 v[62:65], v[26:27], off offset:512
	global_load_dwordx4 v[66:69], v[30:31], off offset:512
	global_load_dwordx4 v[0:3], v[16:17], off offset:512
	global_load_dwordx4 v[4:7], v[20:21], off offset:512
	global_load_dwordx4 v[8:11], v[24:25], off offset:512
	global_load_dwordx4 v[12:15], v[28:29], off offset:512
	ds_read_b128 v[70:73], v42
	ds_read_b128 v[74:77], v43
	ds_read_b128 v[78:81], v42 offset:5376
	ds_read_b128 v[82:85], v43 offset:5376
	ds_read_b128 v[120:123], v42 offset:64
	ds_read_b128 v[124:127], v43 offset:64
	ds_read_b128 v[128:131], v42 offset:5440
	ds_read_b128 v[132:135], v43 offset:5440
	s_waitcnt lgkmcnt(6)
	v_mfma_f32_16x16x32_f16 a[12:15], v[70:73], v[74:77], a[12:15]
	s_waitcnt lgkmcnt(4)
	v_mfma_f32_16x16x32_f16 a[8:11], v[70:73], v[82:85], a[8:11]
	v_mfma_f32_16x16x32_f16 a[4:7], v[78:81], v[74:77], a[4:7]
	v_mfma_f32_16x16x32_f16 a[0:3], v[78:81], v[82:85], a[0:3]
	ds_read_b128 v[70:73], v42 offset:128
	ds_read_b128 v[74:77], v43 offset:128
	ds_read_b128 v[78:81], v42 offset:5504
	ds_read_b128 v[82:85], v43 offset:5504
	s_waitcnt lgkmcnt(6)
	v_mfma_f32_16x16x32_f16 a[12:15], v[120:123], v[124:127], a[12:15]
	s_waitcnt lgkmcnt(4)
	v_mfma_f32_16x16x32_f16 a[8:11], v[120:123], v[132:135], a[8:11]
	v_mfma_f32_16x16x32_f16 a[4:7], v[128:131], v[124:127], a[4:7]
	v_mfma_f32_16x16x32_f16 a[0:3], v[128:131], v[132:135], a[0:3]
	ds_read_b128 v[120:123], v42 offset:192
	ds_read_b128 v[124:127], v43 offset:192
	ds_read_b128 v[128:131], v42 offset:5568
	ds_read_b128 v[132:135], v43 offset:5568
	s_waitcnt lgkmcnt(6)
	v_mfma_f32_16x16x32_f16 a[12:15], v[70:73], v[74:77], a[12:15]
	s_waitcnt lgkmcnt(4)
	v_mfma_f32_16x16x32_f16 a[8:11], v[70:73], v[82:85], a[8:11]
	v_mfma_f32_16x16x32_f16 a[4:7], v[78:81], v[74:77], a[4:7]
	v_mfma_f32_16x16x32_f16 a[0:3], v[78:81], v[82:85], a[0:3]
	s_waitcnt lgkmcnt(2)
	v_mfma_f32_16x16x32_f16 a[12:15], v[120:123], v[124:127], a[12:15]
	s_waitcnt lgkmcnt(0)
	v_mfma_f32_16x16x32_f16 a[8:11], v[120:123], v[132:135], a[8:11]
	v_mfma_f32_16x16x32_f16 a[4:7], v[128:131], v[124:127], a[4:7]
	v_mfma_f32_16x16x32_f16 a[0:3], v[128:131], v[132:135], a[0:3]
	s_barrier
	s_waitcnt vmcnt(14)
	ds_write_b128 v41, v[104:107]
	ds_write_b128 v41, v[108:111] offset:5376
	s_waitcnt vmcnt(12)
	ds_write_b128 v41, v[112:115] offset:10752
	ds_write_b128 v41, v[116:119] offset:16128
	s_waitcnt vmcnt(10)
	ds_write_b128 v40, v[88:91]
	ds_write_b128 v40, v[92:95] offset:5376
	s_waitcnt vmcnt(8)
	ds_write_b128 v40, v[96:99] offset:10752
	ds_write_b128 v40, v[100:103] offset:16128
	s_waitcnt lgkmcnt(0)
	s_barrier
	global_load_dwordx4 v[104:107], v[18:19], off offset:768
	global_load_dwordx4 v[108:111], v[22:23], off offset:768
	global_load_dwordx4 v[112:115], v[26:27], off offset:768
	global_load_dwordx4 v[116:119], v[30:31], off offset:768
	global_load_dwordx4 v[88:91], v[16:17], off offset:768
	global_load_dwordx4 v[92:95], v[20:21], off offset:768
	global_load_dwordx4 v[96:99], v[24:25], off offset:768
	global_load_dwordx4 v[100:103], v[28:29], off offset:768
	ds_read_b128 v[70:73], v42
	ds_read_b128 v[74:77], v43
	ds_read_b128 v[78:81], v42 offset:5376
	ds_read_b128 v[82:85], v43 offset:5376
	ds_read_b128 v[120:123], v42 offset:64
	ds_read_b128 v[124:127], v43 offset:64
	ds_read_b128 v[128:131], v42 offset:5440
	ds_read_b128 v[132:135], v43 offset:5440
	s_waitcnt lgkmcnt(6)
	v_mfma_f32_16x16x32_f16 a[12:15], v[70:73], v[74:77], a[12:15]
	s_waitcnt lgkmcnt(4)
	v_mfma_f32_16x16x32_f16 a[8:11], v[70:73], v[82:85], a[8:11]
	v_mfma_f32_16x16x32_f16 a[4:7], v[78:81], v[74:77], a[4:7]
	v_mfma_f32_16x16x32_f16 a[0:3], v[78:81], v[82:85], a[0:3]
	ds_read_b128 v[70:73], v42 offset:128
	ds_read_b128 v[74:77], v43 offset:128
	ds_read_b128 v[78:81], v42 offset:5504
	ds_read_b128 v[82:85], v43 offset:5504
	s_waitcnt lgkmcnt(6)
	v_mfma_f32_16x16x32_f16 a[12:15], v[120:123], v[124:127], a[12:15]
	s_waitcnt lgkmcnt(4)
	v_mfma_f32_16x16x32_f16 a[8:11], v[120:123], v[132:135], a[8:11]
	v_mfma_f32_16x16x32_f16 a[4:7], v[128:131], v[124:127], a[4:7]
	v_mfma_f32_16x16x32_f16 a[0:3], v[128:131], v[132:135], a[0:3]
	ds_read_b128 v[120:123], v42 offset:192
	ds_read_b128 v[124:127], v43 offset:192
	ds_read_b128 v[128:131], v42 offset:5568
	ds_read_b128 v[132:135], v43 offset:5568
	s_waitcnt lgkmcnt(6)
	v_mfma_f32_16x16x32_f16 a[12:15], v[70:73], v[74:77], a[12:15]
	s_waitcnt lgkmcnt(4)
	v_mfma_f32_16x16x32_f16 a[8:11], v[70:73], v[82:85], a[8:11]
	v_mfma_f32_16x16x32_f16 a[4:7], v[78:81], v[74:77], a[4:7]
	v_mfma_f32_16x16x32_f16 a[0:3], v[78:81], v[82:85], a[0:3]
	s_waitcnt lgkmcnt(2)
	v_mfma_f32_16x16x32_f16 a[12:15], v[120:123], v[124:127], a[12:15]
	s_waitcnt lgkmcnt(0)
	v_mfma_f32_16x16x32_f16 a[8:11], v[120:123], v[132:135], a[8:11]
	v_mfma_f32_16x16x32_f16 a[4:7], v[128:131], v[124:127], a[4:7]
	v_mfma_f32_16x16x32_f16 a[0:3], v[128:131], v[132:135], a[0:3]
	s_barrier
	s_waitcnt vmcnt(14)
	ds_write_b128 v41, v[54:57]
	ds_write_b128 v41, v[58:61] offset:5376
	s_waitcnt vmcnt(12)
	ds_write_b128 v41, v[62:65] offset:10752
	ds_write_b128 v41, v[66:69] offset:16128
	s_waitcnt vmcnt(10)
	ds_write_b128 v40, v[0:3]
	ds_write_b128 v40, v[4:7] offset:5376
	s_waitcnt vmcnt(8)
	ds_write_b128 v40, v[8:11] offset:10752
	ds_write_b128 v40, v[12:15] offset:16128
	s_waitcnt lgkmcnt(0)
	s_barrier
	global_load_dwordx4 v[54:57], v[18:19], off offset:1024
	global_load_dwordx4 v[58:61], v[22:23], off offset:1024
	global_load_dwordx4 v[62:65], v[26:27], off offset:1024
	global_load_dwordx4 v[66:69], v[30:31], off offset:1024
	global_load_dwordx4 v[0:3], v[16:17], off offset:1024
	global_load_dwordx4 v[4:7], v[20:21], off offset:1024
	global_load_dwordx4 v[8:11], v[24:25], off offset:1024
	global_load_dwordx4 v[12:15], v[28:29], off offset:1024
	ds_read_b128 v[70:73], v42
	ds_read_b128 v[74:77], v43
	ds_read_b128 v[78:81], v42 offset:5376
	ds_read_b128 v[82:85], v43 offset:5376
	ds_read_b128 v[120:123], v42 offset:64
	ds_read_b128 v[124:127], v43 offset:64
	ds_read_b128 v[128:131], v42 offset:5440
	ds_read_b128 v[132:135], v43 offset:5440
	s_waitcnt lgkmcnt(6)
	v_mfma_f32_16x16x32_f16 a[12:15], v[70:73], v[74:77], a[12:15]
	s_waitcnt lgkmcnt(4)
	v_mfma_f32_16x16x32_f16 a[8:11], v[70:73], v[82:85], a[8:11]
	v_mfma_f32_16x16x32_f16 a[4:7], v[78:81], v[74:77], a[4:7]
	v_mfma_f32_16x16x32_f16 a[0:3], v[78:81], v[82:85], a[0:3]
	ds_read_b128 v[70:73], v42 offset:128
	ds_read_b128 v[74:77], v43 offset:128
	ds_read_b128 v[78:81], v42 offset:5504
	ds_read_b128 v[82:85], v43 offset:5504
	s_waitcnt lgkmcnt(6)
	v_mfma_f32_16x16x32_f16 a[12:15], v[120:123], v[124:127], a[12:15]
	s_waitcnt lgkmcnt(4)
	v_mfma_f32_16x16x32_f16 a[8:11], v[120:123], v[132:135], a[8:11]
	v_mfma_f32_16x16x32_f16 a[4:7], v[128:131], v[124:127], a[4:7]
	v_mfma_f32_16x16x32_f16 a[0:3], v[128:131], v[132:135], a[0:3]
	ds_read_b128 v[120:123], v42 offset:192
	ds_read_b128 v[124:127], v43 offset:192
	ds_read_b128 v[128:131], v42 offset:5568
	ds_read_b128 v[132:135], v43 offset:5568
	s_waitcnt lgkmcnt(6)
	v_mfma_f32_16x16x32_f16 a[12:15], v[70:73], v[74:77], a[12:15]
	s_waitcnt lgkmcnt(4)
	v_mfma_f32_16x16x32_f16 a[8:11], v[70:73], v[82:85], a[8:11]
	v_mfma_f32_16x16x32_f16 a[4:7], v[78:81], v[74:77], a[4:7]
	v_mfma_f32_16x16x32_f16 a[0:3], v[78:81], v[82:85], a[0:3]
	s_waitcnt lgkmcnt(2)
	v_mfma_f32_16x16x32_f16 a[12:15], v[120:123], v[124:127], a[12:15]
	s_waitcnt lgkmcnt(0)
	v_mfma_f32_16x16x32_f16 a[8:11], v[120:123], v[132:135], a[8:11]
	v_mfma_f32_16x16x32_f16 a[4:7], v[128:131], v[124:127], a[4:7]
	v_mfma_f32_16x16x32_f16 a[0:3], v[128:131], v[132:135], a[0:3]
	s_barrier
	s_waitcnt vmcnt(14)
	ds_write_b128 v41, v[104:107]
	ds_write_b128 v41, v[108:111] offset:5376
	s_waitcnt vmcnt(12)
	ds_write_b128 v41, v[112:115] offset:10752
	ds_write_b128 v41, v[116:119] offset:16128
	s_waitcnt vmcnt(10)
	ds_write_b128 v40, v[88:91]
	ds_write_b128 v40, v[92:95] offset:5376
	s_waitcnt vmcnt(8)
	ds_write_b128 v40, v[96:99] offset:10752
	ds_write_b128 v40, v[100:103] offset:16128
	s_waitcnt lgkmcnt(0)
	s_barrier
	global_load_dwordx4 v[104:107], v[18:19], off offset:1280
	global_load_dwordx4 v[108:111], v[22:23], off offset:1280
	global_load_dwordx4 v[112:115], v[26:27], off offset:1280
	global_load_dwordx4 v[116:119], v[30:31], off offset:1280
	global_load_dwordx4 v[88:91], v[16:17], off offset:1280
	global_load_dwordx4 v[92:95], v[20:21], off offset:1280
	global_load_dwordx4 v[96:99], v[24:25], off offset:1280
	global_load_dwordx4 v[100:103], v[28:29], off offset:1280
	ds_read_b128 v[70:73], v42
	ds_read_b128 v[74:77], v43
	ds_read_b128 v[78:81], v42 offset:5376
	ds_read_b128 v[82:85], v43 offset:5376
	ds_read_b128 v[120:123], v42 offset:64
	ds_read_b128 v[124:127], v43 offset:64
	ds_read_b128 v[128:131], v42 offset:5440
	ds_read_b128 v[132:135], v43 offset:5440
	s_waitcnt lgkmcnt(6)
	v_mfma_f32_16x16x32_f16 a[12:15], v[70:73], v[74:77], a[12:15]
	s_waitcnt lgkmcnt(4)
	v_mfma_f32_16x16x32_f16 a[8:11], v[70:73], v[82:85], a[8:11]
	v_mfma_f32_16x16x32_f16 a[4:7], v[78:81], v[74:77], a[4:7]
	v_mfma_f32_16x16x32_f16 a[0:3], v[78:81], v[82:85], a[0:3]
	ds_read_b128 v[70:73], v42 offset:128
	ds_read_b128 v[74:77], v43 offset:128
	ds_read_b128 v[78:81], v42 offset:5504
	ds_read_b128 v[82:85], v43 offset:5504
	s_waitcnt lgkmcnt(6)
	v_mfma_f32_16x16x32_f16 a[12:15], v[120:123], v[124:127], a[12:15]
	s_waitcnt lgkmcnt(4)
	v_mfma_f32_16x16x32_f16 a[8:11], v[120:123], v[132:135], a[8:11]
	v_mfma_f32_16x16x32_f16 a[4:7], v[128:131], v[124:127], a[4:7]
	v_mfma_f32_16x16x32_f16 a[0:3], v[128:131], v[132:135], a[0:3]
	ds_read_b128 v[120:123], v42 offset:192
	ds_read_b128 v[124:127], v43 offset:192
	ds_read_b128 v[128:131], v42 offset:5568
	ds_read_b128 v[132:135], v43 offset:5568
	s_waitcnt lgkmcnt(6)
	v_mfma_f32_16x16x32_f16 a[12:15], v[70:73], v[74:77], a[12:15]
	s_waitcnt lgkmcnt(4)
	v_mfma_f32_16x16x32_f16 a[8:11], v[70:73], v[82:85], a[8:11]
	v_mfma_f32_16x16x32_f16 a[4:7], v[78:81], v[74:77], a[4:7]
	v_mfma_f32_16x16x32_f16 a[0:3], v[78:81], v[82:85], a[0:3]
	s_waitcnt lgkmcnt(2)
	v_mfma_f32_16x16x32_f16 a[12:15], v[120:123], v[124:127], a[12:15]
	s_waitcnt lgkmcnt(0)
	v_mfma_f32_16x16x32_f16 a[8:11], v[120:123], v[132:135], a[8:11]
	v_mfma_f32_16x16x32_f16 a[4:7], v[128:131], v[124:127], a[4:7]
	v_mfma_f32_16x16x32_f16 a[0:3], v[128:131], v[132:135], a[0:3]
	s_barrier
	s_waitcnt vmcnt(14)
	ds_write_b128 v41, v[54:57]
	ds_write_b128 v41, v[58:61] offset:5376
	s_waitcnt vmcnt(12)
	ds_write_b128 v41, v[62:65] offset:10752
	ds_write_b128 v41, v[66:69] offset:16128
	s_waitcnt vmcnt(10)
	ds_write_b128 v40, v[0:3]
	ds_write_b128 v40, v[4:7] offset:5376
	s_waitcnt vmcnt(8)
	ds_write_b128 v40, v[8:11] offset:10752
	ds_write_b128 v40, v[12:15] offset:16128
	s_waitcnt lgkmcnt(0)
	s_barrier
	global_load_dwordx4 v[54:57], v[18:19], off offset:1536
	global_load_dwordx4 v[58:61], v[22:23], off offset:1536
	global_load_dwordx4 v[62:65], v[26:27], off offset:1536
	global_load_dwordx4 v[66:69], v[30:31], off offset:1536
	global_load_dwordx4 v[0:3], v[16:17], off offset:1536
	global_load_dwordx4 v[4:7], v[20:21], off offset:1536
	global_load_dwordx4 v[8:11], v[24:25], off offset:1536
	global_load_dwordx4 v[12:15], v[28:29], off offset:1536
	ds_read_b128 v[70:73], v42
	ds_read_b128 v[74:77], v43
	ds_read_b128 v[78:81], v42 offset:5376
	ds_read_b128 v[82:85], v43 offset:5376
	ds_read_b128 v[120:123], v42 offset:64
	ds_read_b128 v[124:127], v43 offset:64
	ds_read_b128 v[128:131], v42 offset:5440
	ds_read_b128 v[132:135], v43 offset:5440
	s_waitcnt lgkmcnt(6)
	v_mfma_f32_16x16x32_f16 a[12:15], v[70:73], v[74:77], a[12:15]
	s_waitcnt lgkmcnt(4)
	v_mfma_f32_16x16x32_f16 a[8:11], v[70:73], v[82:85], a[8:11]
	v_mfma_f32_16x16x32_f16 a[4:7], v[78:81], v[74:77], a[4:7]
	v_mfma_f32_16x16x32_f16 a[0:3], v[78:81], v[82:85], a[0:3]
	ds_read_b128 v[70:73], v42 offset:128
	ds_read_b128 v[74:77], v43 offset:128
	ds_read_b128 v[78:81], v42 offset:5504
	ds_read_b128 v[82:85], v43 offset:5504
	s_waitcnt lgkmcnt(6)
	v_mfma_f32_16x16x32_f16 a[12:15], v[120:123], v[124:127], a[12:15]
	s_waitcnt lgkmcnt(4)
	v_mfma_f32_16x16x32_f16 a[8:11], v[120:123], v[132:135], a[8:11]
	v_mfma_f32_16x16x32_f16 a[4:7], v[128:131], v[124:127], a[4:7]
	v_mfma_f32_16x16x32_f16 a[0:3], v[128:131], v[132:135], a[0:3]
	ds_read_b128 v[120:123], v42 offset:192
	ds_read_b128 v[124:127], v43 offset:192
	ds_read_b128 v[128:131], v42 offset:5568
	ds_read_b128 v[132:135], v43 offset:5568
	s_waitcnt lgkmcnt(6)
	v_mfma_f32_16x16x32_f16 a[12:15], v[70:73], v[74:77], a[12:15]
	s_waitcnt lgkmcnt(4)
	v_mfma_f32_16x16x32_f16 a[8:11], v[70:73], v[82:85], a[8:11]
	v_mfma_f32_16x16x32_f16 a[4:7], v[78:81], v[74:77], a[4:7]
	v_mfma_f32_16x16x32_f16 a[0:3], v[78:81], v[82:85], a[0:3]
	s_waitcnt lgkmcnt(2)
	v_mfma_f32_16x16x32_f16 a[12:15], v[120:123], v[124:127], a[12:15]
	s_waitcnt lgkmcnt(0)
	v_mfma_f32_16x16x32_f16 a[8:11], v[120:123], v[132:135], a[8:11]
	v_mfma_f32_16x16x32_f16 a[4:7], v[128:131], v[124:127], a[4:7]
	v_mfma_f32_16x16x32_f16 a[0:3], v[128:131], v[132:135], a[0:3]
	s_barrier
	s_waitcnt vmcnt(14)
	ds_write_b128 v41, v[104:107]
	ds_write_b128 v41, v[108:111] offset:5376
	s_waitcnt vmcnt(12)
	ds_write_b128 v41, v[112:115] offset:10752
	ds_write_b128 v41, v[116:119] offset:16128
	s_waitcnt vmcnt(10)
	ds_write_b128 v40, v[88:91]
	ds_write_b128 v40, v[92:95] offset:5376
	s_waitcnt vmcnt(8)
	ds_write_b128 v40, v[96:99] offset:10752
	ds_write_b128 v40, v[100:103] offset:16128
	s_waitcnt lgkmcnt(0)
	s_barrier
	ds_read_b128 v[70:73], v42
	ds_read_b128 v[74:77], v43
	ds_read_b128 v[78:81], v42 offset:5376
	ds_read_b128 v[82:85], v43 offset:5376
	ds_read_b128 v[120:123], v42 offset:64
	ds_read_b128 v[124:127], v43 offset:64
	ds_read_b128 v[128:131], v42 offset:5440
	ds_read_b128 v[132:135], v43 offset:5440
	s_waitcnt lgkmcnt(6)
	v_mfma_f32_16x16x32_f16 a[12:15], v[70:73], v[74:77], a[12:15]
	s_waitcnt lgkmcnt(4)
	v_mfma_f32_16x16x32_f16 a[8:11], v[70:73], v[82:85], a[8:11]
	v_mfma_f32_16x16x32_f16 a[4:7], v[78:81], v[74:77], a[4:7]
	v_mfma_f32_16x16x32_f16 a[0:3], v[78:81], v[82:85], a[0:3]
	ds_read_b128 v[70:73], v42 offset:128
	ds_read_b128 v[74:77], v43 offset:128
	ds_read_b128 v[78:81], v42 offset:5504
	ds_read_b128 v[82:85], v43 offset:5504
	s_waitcnt lgkmcnt(6)
	v_mfma_f32_16x16x32_f16 a[12:15], v[120:123], v[124:127], a[12:15]
	s_waitcnt lgkmcnt(4)
	v_mfma_f32_16x16x32_f16 a[8:11], v[120:123], v[132:135], a[8:11]
	v_mfma_f32_16x16x32_f16 a[4:7], v[128:131], v[124:127], a[4:7]
	v_mfma_f32_16x16x32_f16 a[0:3], v[128:131], v[132:135], a[0:3]
	ds_read_b128 v[120:123], v42 offset:192
	ds_read_b128 v[124:127], v43 offset:192
	ds_read_b128 v[128:131], v42 offset:5568
	ds_read_b128 v[132:135], v43 offset:5568
	s_waitcnt lgkmcnt(6)
	v_mfma_f32_16x16x32_f16 a[12:15], v[70:73], v[74:77], a[12:15]
	s_waitcnt lgkmcnt(4)
	v_mfma_f32_16x16x32_f16 a[8:11], v[70:73], v[82:85], a[8:11]
	v_mfma_f32_16x16x32_f16 a[4:7], v[78:81], v[74:77], a[4:7]
	v_mfma_f32_16x16x32_f16 a[0:3], v[78:81], v[82:85], a[0:3]
	s_waitcnt lgkmcnt(2)
	v_mfma_f32_16x16x32_f16 a[12:15], v[120:123], v[124:127], a[12:15]
	s_waitcnt lgkmcnt(0)
	v_mfma_f32_16x16x32_f16 a[8:11], v[120:123], v[132:135], a[8:11]
	v_mfma_f32_16x16x32_f16 a[4:7], v[128:131], v[124:127], a[4:7]
	v_mfma_f32_16x16x32_f16 a[0:3], v[128:131], v[132:135], a[0:3]
	s_barrier
	s_waitcnt vmcnt(6)
	ds_write_b128 v41, v[54:57]
	ds_write_b128 v41, v[58:61] offset:5376
	s_waitcnt vmcnt(4)
	ds_write_b128 v41, v[62:65] offset:10752
	ds_write_b128 v41, v[66:69] offset:16128
	s_waitcnt vmcnt(2)
	ds_write_b128 v40, v[0:3]
	ds_write_b128 v40, v[4:7] offset:5376
	s_waitcnt vmcnt(0)
	ds_write_b128 v40, v[8:11] offset:10752
	ds_write_b128 v40, v[12:15] offset:16128
	ds_write_b128 v38, v[46:49] offset:256
	ds_write_b128 v39, v[50:53] offset:256
	s_waitcnt lgkmcnt(0)
	s_barrier
	ds_read_b128 v[70:73], v42
	ds_read_b128 v[74:77], v43
	ds_read_b128 v[78:81], v42 offset:5376
	ds_read_b128 v[82:85], v43 offset:5376
	ds_read_b128 v[120:123], v42 offset:64
	ds_read_b128 v[124:127], v43 offset:64
	ds_read_b128 v[128:131], v42 offset:5440
	ds_read_b128 v[132:135], v43 offset:5440
	s_waitcnt lgkmcnt(6)
	v_mfma_f32_16x16x32_f16 a[12:15], v[70:73], v[74:77], a[12:15]
	s_waitcnt lgkmcnt(4)
	v_mfma_f32_16x16x32_f16 a[8:11], v[70:73], v[82:85], a[8:11]
	v_mfma_f32_16x16x32_f16 a[4:7], v[78:81], v[74:77], a[4:7]
	v_mfma_f32_16x16x32_f16 a[0:3], v[78:81], v[82:85], a[0:3]
	ds_read_b128 v[70:73], v42 offset:128
	ds_read_b128 v[74:77], v43 offset:128
	ds_read_b128 v[78:81], v42 offset:5504
	ds_read_b128 v[82:85], v43 offset:5504
	s_waitcnt lgkmcnt(6)
	v_mfma_f32_16x16x32_f16 a[12:15], v[120:123], v[124:127], a[12:15]
	s_waitcnt lgkmcnt(4)
	v_mfma_f32_16x16x32_f16 a[8:11], v[120:123], v[132:135], a[8:11]
	v_mfma_f32_16x16x32_f16 a[4:7], v[128:131], v[124:127], a[4:7]
	v_mfma_f32_16x16x32_f16 a[0:3], v[128:131], v[132:135], a[0:3]
	ds_read_b128 v[120:123], v42 offset:192
	ds_read_b128 v[124:127], v43 offset:192
	ds_read_b128 v[128:131], v42 offset:5568
	ds_read_b128 v[132:135], v43 offset:5568
	s_waitcnt lgkmcnt(6)
	v_mfma_f32_16x16x32_f16 a[12:15], v[70:73], v[74:77], a[12:15]
	s_waitcnt lgkmcnt(4)
	v_mfma_f32_16x16x32_f16 a[8:11], v[70:73], v[82:85], a[8:11]
	v_mfma_f32_16x16x32_f16 a[4:7], v[78:81], v[74:77], a[4:7]
	v_mfma_f32_16x16x32_f16 a[0:3], v[78:81], v[82:85], a[0:3]
	ds_read_b128 v[70:73], v42 offset:256
	ds_read_b128 v[74:77], v43 offset:256
	ds_read_b128 v[78:81], v42 offset:5632
	ds_read_b128 v[82:85], v43 offset:5632
	s_waitcnt lgkmcnt(6)
	v_mfma_f32_16x16x32_f16 a[12:15], v[120:123], v[124:127], a[12:15]
	s_waitcnt lgkmcnt(4)
	v_mfma_f32_16x16x32_f16 a[8:11], v[120:123], v[132:135], a[8:11]
	v_mfma_f32_16x16x32_f16 a[4:7], v[128:131], v[124:127], a[4:7]
	v_mfma_f32_16x16x32_f16 a[0:3], v[128:131], v[132:135], a[0:3]
	s_waitcnt lgkmcnt(2)
	v_mfma_f32_16x16x32_f16 a[12:15], v[70:73], v[74:77], a[12:15]
	s_waitcnt lgkmcnt(0)
	v_mfma_f32_16x16x32_f16 a[8:11], v[70:73], v[82:85], a[8:11]
	v_mfma_f32_16x16x32_f16 a[4:7], v[78:81], v[74:77], a[4:7]
	v_mfma_f32_16x16x32_f16 a[0:3], v[78:81], v[82:85], a[0:3]
	s_barrier
	s_waitcnt vmcnt(4)
	v_mov_b32_e32 v3, v34
	v_mov_b32_e32 v2, v35

	.amdhsa_kernel _Z15gemm_f16_kernelPKDF16_S0_PKfS2_Pfiiiiiii
		.amdhsa_group_segment_fixed_size 43008
		.amdhsa_private_segment_fixed_size 0
		.amdhsa_kernarg_size 68
		.amdhsa_user_sgpr_count 2
		.amdhsa_user_sgpr_dispatch_ptr 0
		.amdhsa_user_sgpr_queue_ptr 0
		.amdhsa_user_sgpr_kernarg_segment_ptr 1
		.amdhsa_user_sgpr_dispatch_id 0
		.amdhsa_user_sgpr_kernarg_preload_length 0
		.amdhsa_user_sgpr_kernarg_preload_offset 0
		.amdhsa_user_sgpr_private_segment_size 0
		.amdhsa_uses_dynamic_stack 0
		.amdhsa_enable_private_segment 0
		.amdhsa_system_sgpr_workgroup_id_x 1
		.amdhsa_system_sgpr_workgroup_id_y 0
		.amdhsa_system_sgpr_workgroup_id_z 0
		.amdhsa_system_sgpr_workgroup_info 0
		.amdhsa_system_vgpr_workitem_id 0
		.amdhsa_next_free_vgpr 152
		.amdhsa_next_free_sgpr 96
		.amdhsa_accum_offset 136
		.amdhsa_reserve_vcc 1
		.amdhsa_float_round_mode_32 0
		.amdhsa_float_round_mode_16_64 0
		.amdhsa_float_denorm_mode_32 3
		.amdhsa_float_denorm_mode_16_64 3
		.amdhsa_dx10_clamp 1
		.amdhsa_ieee_mode 1
		.amdhsa_fp16_overflow 0
		.amdhsa_tg_split 0
		.amdhsa_exception_fp_ieee_invalid_op 0
		.amdhsa_exception_fp_denorm_src 0
		.amdhsa_exception_fp_ieee_div_zero 0
		.amdhsa_exception_fp_ieee_overflow 0
		.amdhsa_exception_fp_ieee_underflow 0
		.amdhsa_exception_fp_ieee_inexact 0
		.amdhsa_exception_int_div_zero 0
	.end_amdhsa_kernel

amdhsa.kernels:
  - .agpr_count:     16
    .args:
      - .actual_access:  read_only
        .address_space:  global
        .offset:         0
        .size:           8
        .value_kind:     global_buffer
      - .actual_access:  read_only
        .address_space:  global
        .offset:         8
        .size:           8
        .value_kind:     global_buffer
      - .actual_access:  read_only
        .address_space:  global
        .offset:         16
        .size:           8
        .value_kind:     global_buffer
      - .actual_access:  read_only
        .address_space:  global
        .offset:         24
        .size:           8
        .value_kind:     global_buffer
      - .actual_access:  write_only
        .address_space:  global
        .offset:         32
        .size:           8
        .value_kind:     global_buffer
      - .offset:         40
        .size:           4
        .value_kind:     by_value
      - .offset:         44
        .size:           4
        .value_kind:     by_value
      - .offset:         48
        .size:           4
        .value_kind:     by_value
      - .offset:         52
        .size:           4
        .value_kind:     by_value
      - .offset:         56
        .size:           4
        .value_kind:     by_value
      - .offset:         60
        .size:           4
        .value_kind:     by_value
      - .offset:         64
        .size:           4
        .value_kind:     by_value
    .group_segment_fixed_size: 43008
    .kernarg_segment_align: 8
    .kernarg_segment_size: 68
    .language:       OpenCL C
    .language_version:
      - 2
      - 0
    .max_flat_workgroup_size: 256
    .name:           _Z15gemm_f16_kernelPKDF16_S0_PKfS2_Pfiiiiiii
    .private_segment_fixed_size: 0
    .sgpr_count:     33
    .sgpr_spill_count: 0
    .symbol:         _Z15gemm_f16_kernelPKDF16_S0_PKfS2_Pfiiiiiii.kd
    .uniform_work_group_size: 1
    .uses_dynamic_stack: false
    .vgpr_count:     152
    .vgpr_spill_count: 0
    .wavefront_size: 64
  - .agpr_count:     0
    .args:
      - .actual_access:  read_only
        .address_space:  global
        .offset:         0
        .size:           8
        .value_kind:     global_buffer
      - .actual_access:  read_only
        .address_space:  global
        .offset:         8
        .size:           8
        .value_kind:     global_buffer
      - .actual_access:  read_only
        .address_space:  global
        .offset:         16
        .size:           8
        .value_kind:     global_buffer
      - .actual_access:  read_only
        .address_space:  global
        .offset:         24
        .size:           8
        .value_kind:     global_buffer
      - .actual_access:  read_only
        .address_space:  global
        .offset:         32
        .size:           8
        .value_kind:     global_buffer
      - .actual_access:  read_only
        .address_space:  global
        .offset:         40
        .size:           8
        .value_kind:     global_buffer
      - .actual_access:  write_only
        .address_space:  global
        .offset:         48
        .size:           8
        .value_kind:     global_buffer
      - .actual_access:  read_only
        .address_space:  global
        .offset:         56
        .size:           8
        .value_kind:     global_buffer
    .group_segment_fixed_size: 121472
    .kernarg_segment_align: 8
    .kernarg_segment_size: 64
    .language:       OpenCL C
    .language_version:
      - 2
      - 0
    .max_flat_workgroup_size: 512
    .name:           _Z15score_ds_kernelPKfS0_S0_S0_S0_S0_PfPKDF16_
    .private_segment_fixed_size: 0
    .sgpr_count:     32
    .sgpr_spill_count: 0
    .symbol:         _Z15score_ds_kernelPKfS0_S0_S0_S0_S0_PfPKDF16_.kd
    .uniform_work_group_size: 1
    .uses_dynamic_stack: false
    .vgpr_count:     254
    .vgpr_spill_count: 0
    .wavefront_size: 64
  - .agpr_count:     0
    .args:
      - .actual_access:  read_only
        .address_space:  global
        .offset:         0
        .size:           8
        .value_kind:     global_buffer
      - .actual_access:  read_only
        .address_space:  global
        .offset:         8
        .size:           8
        .value_kind:     global_buffer
      - .actual_access:  read_only
        .address_space:  global
        .offset:         16
        .size:           8
        .value_kind:     global_buffer
      - .actual_access:  read_only
        .address_space:  global
        .offset:         24
        .size:           8
        .value_kind:     global_buffer
      - .actual_access:  read_only
        .address_space:  global
        .offset:         32
        .size:           8
        .value_kind:     global_buffer
      - .actual_access:  read_only
        .address_space:  global
        .offset:         40
        .size:           8
        .value_kind:     global_buffer
      - .actual_access:  read_only
        .address_space:  global
        .offset:         48
        .size:           8
        .value_kind:     global_buffer
      - .actual_access:  read_only
        .address_space:  global
        .offset:         56
        .size:           8
        .value_kind:     global_buffer
      - .actual_access:  read_only
        .address_space:  global
        .offset:         64
        .size:           8
        .value_kind:     global_buffer
      - .actual_access:  read_only
        .address_space:  global
        .offset:         72
        .size:           8
        .value_kind:     global_buffer
      - .actual_access:  write_only
        .address_space:  global
        .offset:         80
        .size:           8
        .value_kind:     global_buffer
    .group_segment_fixed_size: 70336
    .kernarg_segment_align: 8
    .kernarg_segment_size: 88
    .language:       OpenCL C
    .language_version:
      - 2
      - 0
    .max_flat_workgroup_size: 1024
    .name:           _Z13attend_kernelPKfS0_S0_S0_S0_S0_S0_S0_S0_S0_PDF16_
    .private_segment_fixed_size: 0
    .sgpr_count:     40
    .sgpr_spill_count: 0
    .symbol:         _Z13attend_kernelPKfS0_S0_S0_S0_S0_S0_S0_S0_S0_PDF16_.kd
    .uniform_work_group_size: 1
    .uses_dynamic_stack: false
    .vgpr_count:     86
    .vgpr_spill_count: 0
    .wavefront_size: 64
  - .agpr_count:     0
    .args:
      - .actual_access:  read_only
        .address_space:  global
        .offset:         0
        .size:           8
        .value_kind:     global_buffer
      - .actual_access:  read_only
        .address_space:  global
        .offset:         8
        .size:           8
        .value_kind:     global_buffer
      - .actual_access:  read_only
        .address_space:  global
        .offset:         16
        .size:           8
        .value_kind:     global_buffer
      - .actual_access:  read_only
        .address_space:  global
        .offset:         24
        .size:           8
        .value_kind:     global_buffer
      - .actual_access:  write_only
        .address_space:  global
        .offset:         32
        .size:           8
        .value_kind:     global_buffer
    .group_segment_fixed_size: 9088
    .kernarg_segment_align: 8
    .kernarg_segment_size: 40
    .language:       OpenCL C
    .language_version:
      - 2
      - 0
    .max_flat_workgroup_size: 512
    .name:           _Z16postfinal_kernelPKfS0_S0_S0_Pf
    .private_segment_fixed_size: 0
    .sgpr_count:     30
    .sgpr_spill_count: 0
    .symbol:         _Z16postfinal_kernelPKfS0_S0_S0_Pf.kd
    .uniform_work_group_size: 1
    .uses_dynamic_stack: false
    .vgpr_count:     124
    .vgpr_spill_count: 0
    .wavefront_size: 64
  - .agpr_count:     16
    .args:
      - .offset:         0
        .size:           1136
        .value_kind:     by_value
    .group_segment_fixed_size: 34816
    .kernarg_segment_align: 8
    .kernarg_segment_size: 1136
    .language:       OpenCL C
    .language_version:
      - 2
      - 0
    .max_flat_workgroup_size: 256
    .name:           _Z14gemm_nt_kernelILi2EEv8GemmArgs
    .private_segment_fixed_size: 0
    .sgpr_count:     68
    .sgpr_spill_count: 0
    .symbol:         _Z14gemm_nt_kernelILi2EEv8GemmArgs.kd
    .uniform_work_group_size: 1
    .uses_dynamic_stack: false
    .vgpr_count:     140
    .vgpr_spill_count: 0
    .wavefront_size: 64
  - .agpr_count:     0
    .args:
      - .actual_access:  read_only
        .address_space:  global
        .offset:         0
        .size:           8
        .value_kind:     global_buffer
      - .offset:         8
        .size:           8
        .value_kind:     by_value
      - .actual_access:  read_only
        .address_space:  global
        .offset:         16
        .size:           8
        .value_kind:     global_buffer
      - .actual_access:  read_only
        .address_space:  global
        .offset:         24
        .size:           8
        .value_kind:     global_buffer
      - .actual_access:  read_only
        .address_space:  global
        .offset:         32
        .size:           8
        .value_kind:     global_buffer
      - .actual_access:  read_only
        .address_space:  global
        .offset:         40
        .size:           8
        .value_kind:     global_buffer
      - .actual_access:  write_only
        .address_space:  global
        .offset:         48
        .size:           8
        .value_kind:     global_buffer
      - .actual_access:  write_only
        .address_space:  global
        .offset:         56
        .size:           8
        .value_kind:     global_buffer
      - .offset:         64
        .size:           4
        .value_kind:     by_value
      - .offset:         72
        .size:           376
        .value_kind:     by_value
    .group_segment_fixed_size: 63488
    .kernarg_segment_align: 8
    .kernarg_segment_size: 448
    .language:       OpenCL C
    .language_version:
      - 2
      - 0
    .max_flat_workgroup_size: 512
    .name:           _Z15gru_mfma_kernelILi1EEvPKfmS1_S1_S1_S1_PfS2_i7PreArgs
    .private_segment_fixed_size: 0
    .sgpr_count:     36
    .sgpr_spill_count: 0
    .symbol:         _Z15gru_mfma_kernelILi1EEvPKfmS1_S1_S1_S1_PfS2_i7PreArgs.kd
    .uniform_work_group_size: 1
    .uses_dynamic_stack: false
    .vgpr_count:     232
    .vgpr_spill_count: 0
    .wavefront_size: 64
  - .agpr_count:     0
    .args:
      - .actual_access:  read_only
        .address_space:  global
        .offset:         0
        .size:           8
        .value_kind:     global_buffer
      - .offset:         8
        .size:           8
        .value_kind:     by_value
      - .actual_access:  read_only
        .address_space:  global
        .offset:         16
        .size:           8
        .value_kind:     global_buffer
      - .actual_access:  read_only
        .address_space:  global
        .offset:         24
        .size:           8
        .value_kind:     global_buffer
      - .actual_access:  read_only
        .address_space:  global
        .offset:         32
        .size:           8
        .value_kind:     global_buffer
      - .actual_access:  read_only
        .address_space:  global
        .offset:         40
        .size:           8
        .value_kind:     global_buffer
      - .actual_access:  write_only
        .address_space:  global
        .offset:         48
        .size:           8
        .value_kind:     global_buffer
      - .actual_access:  write_only
        .address_space:  global
        .offset:         56
        .size:           8
        .value_kind:     global_buffer
      - .offset:         64
        .size:           4
        .value_kind:     by_value
      - .offset:         72
        .size:           376
        .value_kind:     by_value
    .group_segment_fixed_size: 64480
    .kernarg_segment_align: 8
    .kernarg_segment_size: 448
    .language:       OpenCL C
    .language_version:
      - 2
      - 0
    .max_flat_workgroup_size: 512
    .name:           _Z15gru_mfma_kernelILi2EEvPKfmS1_S1_S1_S1_PfS2_i7PreArgs
    .private_segment_fixed_size: 0
    .sgpr_count:     50
    .sgpr_spill_count: 0
    .symbol:         _Z15gru_mfma_kernelILi2EEvPKfmS1_S1_S1_S1_PfS2_i7PreArgs.kd
    .uniform_work_group_size: 1
    .uses_dynamic_stack: false
    .vgpr_count:     232
    .vgpr_spill_count: 0
    .wavefront_size: 64
